# speedup vs baseline: 1.0282x; 1.0053x over previous
.LBB0_34:
	s_waitcnt vmcnt(0)
	v_ashrrev_i32_e32 v1, 8, v6
	v_ashrrev_i32_e32 v26, 8, v7
	v_ashrrev_i32_e32 v27, 8, v8
	v_ashrrev_i32_e32 v28, 8, v9
	v_lshlrev_b32_e32 v1, 2, v1
	v_lshlrev_b32_e32 v26, 2, v26
	v_lshlrev_b32_e32 v27, 2, v27
	v_lshlrev_b32_e32 v28, 2, v28
	ds_read_b32 v1, v1 offset:1564
	ds_read_b32 v26, v26 offset:1564
	ds_read_b32 v27, v27 offset:1564
	ds_read_b32 v28, v28 offset:1564
	s_mov_b32 s8, 0x1fe0000
	v_lshlrev_b32_e32 v6, 17, v6
	v_lshlrev_b32_e32 v7, 17, v7
	v_lshlrev_b32_e32 v8, 17, v8
	v_lshlrev_b32_e32 v9, 17, v9
	v_and_or_b32 v6, v6, s8, v10
	v_and_or_b32 v7, v7, s8, v11
	v_and_or_b32 v8, v8, s8, v12
	v_and_or_b32 v9, v9, s8, v13
	v_lshlrev_b32_e32 v41, 3, v41
	v_lshlrev_b32_e32 v37, 3, v37
	v_lshlrev_b32_e32 v42, 3, v42
	v_lshlrev_b32_e32 v39, 3, v39
	v_mov_b32_e32 v31, v2
	v_mov_b32_e32 v33, v4
	v_mov_b32_e32 v30, v6
	v_mov_b32_e32 v32, v8
	v_mov_b32_e32 v2, v7
	v_mov_b32_e32 v4, v9
	s_waitcnt lgkmcnt(3)
	v_lshl_add_u32 v1, v1, 3, v41
	s_waitcnt lgkmcnt(2)
	v_lshl_add_u32 v26, v26, 3, v37
	s_waitcnt lgkmcnt(1)
	v_lshl_add_u32 v27, v27, 3, v42
	s_waitcnt lgkmcnt(0)
	v_lshl_add_u32 v28, v28, 3, v39
	ds_write_b64 v1, v[30:31] offset:8192
	ds_write_b64 v26, v[2:3] offset:8192
	ds_write_b64 v27, v[32:33] offset:8192
	ds_write_b64 v28, v[4:5] offset:8192
.LBB0_35:
	s_or_b64 exec, exec, s[6:7]
	v_lshlrev_b32_e32 v1, 3, v0
	s_waitcnt lgkmcnt(0)
	s_barrier
	s_waitcnt vmcnt(0)
	ds_read_b64 v[4:5], v1 offset:8192
	ds_read_b64 v[6:7], v1 offset:12288
	ds_read_b64 v[8:9], v1 offset:16384
	ds_read_b64 v[10:11], v1 offset:20480
	ds_read_b64 v[12:13], v1 offset:24576
	ds_read_b64 v[14:15], v1 offset:28672
	ds_read_b64 v[16:17], v1 offset:32768
	ds_read_b64 v[18:19], v1 offset:36864
	v_add_u32_e32 v2, s10, v0
	v_lshlrev_b32_e32 v2, 3, v2
	v_add_u32_e32 v20, 0x1000, v2
	v_add_u32_e32 v21, 0x2000, v2
	v_add_u32_e32 v22, 0x3000, v2
	v_add_u32_e32 v23, 0x4000, v2
	v_add_u32_e32 v24, 0x5000, v2
	v_add_u32_e32 v25, 0x6000, v2
	v_add_u32_e32 v26, 0x7000, v2
	s_waitcnt lgkmcnt(7)
	global_store_dwordx2 v2, v[4:5], s[4:5]
	s_mov_b64 s[6:7], exec
	v_or_b32_e32 v3, 0x200, v0
	v_cmp_gt_u32_e32 vcc, s3, v3
	s_and_b64 exec, exec, vcc
	s_cbranch_execz .LBB0_43
	s_waitcnt lgkmcnt(6)
	global_store_dwordx2 v20, v[6:7], s[4:5]
	v_or_b32_e32 v3, 0x400, v0
	v_cmp_gt_u32_e32 vcc, s3, v3
	s_and_b64 exec, exec, vcc
	s_cbranch_execz .LBB0_43
	s_waitcnt lgkmcnt(5)
	global_store_dwordx2 v21, v[8:9], s[4:5]
	v_or_b32_e32 v3, 0x600, v0
	v_cmp_gt_u32_e32 vcc, s3, v3
	s_and_b64 exec, exec, vcc
	s_cbranch_execz .LBB0_43
	s_waitcnt lgkmcnt(4)
	global_store_dwordx2 v22, v[10:11], s[4:5]
	v_or_b32_e32 v3, 0x800, v0
	v_cmp_gt_u32_e32 vcc, s3, v3
	s_and_b64 exec, exec, vcc
	s_cbranch_execz .LBB0_43
	s_waitcnt lgkmcnt(3)
	global_store_dwordx2 v23, v[12:13], s[4:5]
	v_or_b32_e32 v3, 0xa00, v0
	v_cmp_gt_u32_e32 vcc, s3, v3
	s_and_b64 exec, exec, vcc
	s_cbranch_execz .LBB0_43
	s_waitcnt lgkmcnt(2)
	global_store_dwordx2 v24, v[14:15], s[4:5]
	v_or_b32_e32 v3, 0xc00, v0
	v_cmp_gt_u32_e32 vcc, s3, v3
	s_and_b64 exec, exec, vcc
	s_cbranch_execz .LBB0_43
	s_waitcnt lgkmcnt(1)
	global_store_dwordx2 v25, v[16:17], s[4:5]
	v_or_b32_e32 v3, 0xe00, v0
	v_cmp_gt_u32_e32 vcc, s3, v3
	s_and_b64 exec, exec, vcc
	s_cbranch_execz .LBB0_43
	s_waitcnt lgkmcnt(0)
	global_store_dwordx2 v26, v[18:19], s[4:5]

.LBB0_48:
	s_waitcnt vmcnt(3)
	v_ashrrev_i32_e32 v1, 8, v18
	v_ashrrev_i32_e32 v26, 8, v19
	v_ashrrev_i32_e32 v27, 8, v20
	v_ashrrev_i32_e32 v28, 8, v21
	v_lshlrev_b32_e32 v1, 2, v1
	v_lshlrev_b32_e32 v26, 2, v26
	v_lshlrev_b32_e32 v27, 2, v27
	v_lshlrev_b32_e32 v28, 2, v28
	ds_read_b32 v1, v1 offset:1564
	ds_read_b32 v26, v26 offset:1564
	ds_read_b32 v27, v27 offset:1564
	ds_read_b32 v28, v28 offset:1564
	s_mov_b32 s6, 0x1fe0000
	v_lshlrev_b32_e32 v18, 17, v18
	v_lshlrev_b32_e32 v19, 17, v19
	v_lshlrev_b32_e32 v20, 17, v20
	v_lshlrev_b32_e32 v21, 17, v21
	v_and_or_b32 v18, v18, s6, v22
	v_and_or_b32 v19, v19, s6, v23
	v_and_or_b32 v20, v20, s6, v24
	v_and_or_b32 v21, v21, s6, v25
	v_lshlrev_b32_e32 v38, 3, v38
	v_lshlrev_b32_e32 v35, 3, v35
	v_lshlrev_b32_e32 v40, 3, v40
	v_lshlrev_b32_e32 v36, 3, v36
	v_mov_b32_e32 v31, v14
	v_mov_b32_e32 v33, v16
	v_mov_b32_e32 v30, v18
	v_mov_b32_e32 v32, v20
	v_mov_b32_e32 v14, v19
	v_mov_b32_e32 v16, v21
	s_waitcnt lgkmcnt(3)
	v_lshl_add_u32 v1, v1, 3, v38
	s_waitcnt lgkmcnt(2)
	v_lshl_add_u32 v26, v26, 3, v35
	s_waitcnt lgkmcnt(1)
	v_lshl_add_u32 v27, v27, 3, v40
	s_waitcnt lgkmcnt(0)
	v_lshl_add_u32 v28, v28, 3, v36
	ds_write_b64 v1, v[30:31] offset:8192
	ds_write_b64 v26, v[14:15] offset:8192
	ds_write_b64 v27, v[32:33] offset:8192
	ds_write_b64 v28, v[16:17] offset:8192
	s_or_b64 exec, exec, s[8:9]
	s_and_saveexec_b64 s[6:7], vcc
	s_cbranch_execnz .LBB0_34
	s_branch .LBB0_35

.LBB1_60:
	s_or_b64 exec, exec, s[6:7]
	s_waitcnt lgkmcnt(0)
	s_barrier
	v_and_b32_e32 v31, 0x1fffc, v31
	v_and_b32_e32 v30, 0x1fffc, v30
	v_and_b32_e32 v33, 0x1fffc, v33
	v_and_b32_e32 v32, 0x1fffc, v32
	v_and_b32_e32 v35, 0x1fffc, v35
	v_and_b32_e32 v26, 0x1fffc, v26
	v_and_b32_e32 v37, 0x1fffc, v37
	v_and_b32_e32 v24, 0x1fffc, v24
	v_and_b32_e32 v39, 0x1fffc, v39
	ds_read_b32 v31, v31 offset:3132
	ds_read_b32 v30, v30 offset:3132
	ds_read_b32 v33, v33 offset:3132
	ds_read_b32 v32, v32 offset:3132
	ds_read_b32 v35, v35 offset:3132
	ds_read_b32 v26, v26 offset:3132
	ds_read_b32 v37, v37 offset:3132
	ds_read_b32 v24, v24 offset:3132
	ds_read_b32 v39, v39 offset:3132
	v_lshlrev_b32_e32 v34, 3, v34
	v_lshlrev_b32_e32 v29, 3, v29
	v_lshlrev_b32_e32 v36, 3, v36
	v_lshlrev_b32_e32 v28, 3, v28
	v_lshlrev_b32_e32 v38, 3, v38
	v_lshlrev_b32_e32 v27, 3, v27
	v_lshlrev_b32_e32 v40, 3, v40
	v_lshlrev_b32_e32 v25, 3, v25
	v_lshlrev_b32_e32 v41, 3, v41
	v_and_b32_e32 v18, 0x1ffff, v18
	v_and_b32_e32 v16, 0x1ffff, v16
	v_and_b32_e32 v12, 0x1ffff, v12
	v_and_b32_e32 v8, 0x1ffff, v8
	v_and_b32_e32 v14, 0x1ffff, v14
	v_and_b32_e32 v10, 0x1ffff, v10
	v_and_b32_e32 v6, 0x1ffff, v6
	v_and_b32_e32 v4, 0x1ffff, v4
	v_and_b32_e32 v2, 0x1ffff, v2
	s_mov_b64 s[4:5], exec
	s_waitcnt lgkmcnt(8)
	s_and_b64 exec, exec, vcc
	v_lshl_add_u32 v31, v31, 3, v34
	ds_write_b64 v31, v[18:19] offset:8192
	s_waitcnt lgkmcnt(7)
	s_and_b64 exec, exec, s[8:9]
	v_lshl_add_u32 v30, v30, 3, v29
	ds_write_b64 v30, v[16:17] offset:8192
	s_waitcnt lgkmcnt(6)
	s_and_b64 exec, exec, s[10:11]
	v_lshl_add_u32 v33, v33, 3, v36
	ds_write_b64 v33, v[12:13] offset:8192
	s_waitcnt lgkmcnt(5)
	s_and_b64 exec, exec, s[12:13]
	v_lshl_add_u32 v32, v32, 3, v28
	ds_write_b64 v32, v[8:9] offset:8192
	s_waitcnt lgkmcnt(4)
	s_and_b64 exec, exec, s[14:15]
	v_lshl_add_u32 v35, v35, 3, v38
	ds_write_b64 v35, v[14:15] offset:8192
	s_waitcnt lgkmcnt(3)
	s_and_b64 exec, exec, s[16:17]
	v_lshl_add_u32 v26, v26, 3, v27
	ds_write_b64 v26, v[10:11] offset:8192
	s_waitcnt lgkmcnt(2)
	s_and_b64 exec, exec, s[18:19]
	v_lshl_add_u32 v37, v37, 3, v40
	ds_write_b64 v37, v[6:7] offset:8192
	s_waitcnt lgkmcnt(1)
	s_and_b64 exec, exec, s[20:21]
	v_lshl_add_u32 v24, v24, 3, v25
	ds_write_b64 v24, v[4:5] offset:8192
	s_waitcnt lgkmcnt(0)
	s_and_b64 exec, exec, s[22:23]
	v_lshl_add_u32 v39, v39, 3, v41
	ds_write_b64 v39, v[2:3] offset:8192

.LBB1_100:
	v_lshrrev_b32_e32 v20, 3, v0
	v_and_b32_e32 v1, 7, v0
	v_lshlrev_b32_e32 v1, 4, v1
	v_or_b32_e32 v24, s46, v20
	v_lshlrev_b32_e32 v20, 2, v20
	s_mov_b32 s2, 0x186a0
	s_waitcnt lgkmcnt(0)
	s_barrier
	ds_read_b32 v26, v20 offset:4220
	ds_read_b32 v28, v20 offset:4476
	ds_read_b32 v30, v20 offset:4732
	ds_read_b32 v32, v20 offset:4988
	v_cvt_f32_f16_e32 v2, v60
	v_cvt_f32_f16_sdwa v3, v60 dst_sel:DWORD dst_unused:UNUSED_PAD src0_sel:WORD_1
	v_cvt_f32_f16_e32 v4, v61
	v_cvt_f32_f16_sdwa v5, v61 dst_sel:DWORD dst_unused:UNUSED_PAD src0_sel:WORD_1
	v_cvt_f32_f16_e32 v6, v62
	v_cvt_f32_f16_sdwa v7, v62 dst_sel:DWORD dst_unused:UNUSED_PAD src0_sel:WORD_1
	v_cvt_f32_f16_e32 v8, v63
	v_cvt_f32_f16_sdwa v9, v63 dst_sel:DWORD dst_unused:UNUSED_PAD src0_sel:WORD_1
	v_add_u32_e32 v10, 0, v24
	s_waitcnt lgkmcnt(3)
	v_pk_mul_f32 v[2:3], v[26:27], v[2:3] op_sel_hi:[0,1]
	v_pk_mul_f32 v[4:5], v[26:27], v[4:5] op_sel_hi:[0,1]
	v_pk_mul_f32 v[6:7], v[26:27], v[6:7] op_sel_hi:[0,1]
	v_pk_mul_f32 v[8:9], v[26:27], v[8:9] op_sel_hi:[0,1]
	v_cmp_gt_u32_e32 vcc, s2, v10
	v_lshl_or_b32 v11, v10, 7, v1
	v_cvt_pk_f16_f32 v60, v2, v3
	v_cvt_pk_f16_f32 v61, v4, v5
	v_cvt_pk_f16_f32 v62, v6, v7
	v_cvt_pk_f16_f32 v63, v8, v9
	s_and_saveexec_b64 s[0:1], vcc
	global_store_dwordx4 v11, v[60:63], s[44:45]
	s_or_b64 exec, exec, s[0:1]
	v_cvt_f32_f16_e32 v2, v64
	v_cvt_f32_f16_sdwa v3, v64 dst_sel:DWORD dst_unused:UNUSED_PAD src0_sel:WORD_1
	v_cvt_f32_f16_e32 v4, v65
	v_cvt_f32_f16_sdwa v5, v65 dst_sel:DWORD dst_unused:UNUSED_PAD src0_sel:WORD_1
	v_cvt_f32_f16_e32 v6, v66
	v_cvt_f32_f16_sdwa v7, v66 dst_sel:DWORD dst_unused:UNUSED_PAD src0_sel:WORD_1
	v_cvt_f32_f16_e32 v8, v67
	v_cvt_f32_f16_sdwa v9, v67 dst_sel:DWORD dst_unused:UNUSED_PAD src0_sel:WORD_1
	v_add_u32_e32 v10, 64, v24
	s_waitcnt lgkmcnt(2)
	v_pk_mul_f32 v[2:3], v[28:29], v[2:3] op_sel_hi:[0,1]
	v_pk_mul_f32 v[4:5], v[28:29], v[4:5] op_sel_hi:[0,1]
	v_pk_mul_f32 v[6:7], v[28:29], v[6:7] op_sel_hi:[0,1]
	v_pk_mul_f32 v[8:9], v[28:29], v[8:9] op_sel_hi:[0,1]
	v_cmp_gt_u32_e32 vcc, s2, v10
	v_lshl_or_b32 v11, v10, 7, v1
	v_cvt_pk_f16_f32 v64, v2, v3
	v_cvt_pk_f16_f32 v65, v4, v5
	v_cvt_pk_f16_f32 v66, v6, v7
	v_cvt_pk_f16_f32 v67, v8, v9
	s_and_saveexec_b64 s[0:1], vcc
	global_store_dwordx4 v11, v[64:67], s[44:45]
	s_or_b64 exec, exec, s[0:1]
	v_cvt_f32_f16_e32 v2, v68
	v_cvt_f32_f16_sdwa v3, v68 dst_sel:DWORD dst_unused:UNUSED_PAD src0_sel:WORD_1
	v_cvt_f32_f16_e32 v4, v69
	v_cvt_f32_f16_sdwa v5, v69 dst_sel:DWORD dst_unused:UNUSED_PAD src0_sel:WORD_1
	v_cvt_f32_f16_e32 v6, v70
	v_cvt_f32_f16_sdwa v7, v70 dst_sel:DWORD dst_unused:UNUSED_PAD src0_sel:WORD_1
	v_cvt_f32_f16_e32 v8, v71
	v_cvt_f32_f16_sdwa v9, v71 dst_sel:DWORD dst_unused:UNUSED_PAD src0_sel:WORD_1
	v_add_u32_e32 v10, 0x80, v24
	s_waitcnt lgkmcnt(1)
	v_pk_mul_f32 v[2:3], v[30:31], v[2:3] op_sel_hi:[0,1]
	v_pk_mul_f32 v[4:5], v[30:31], v[4:5] op_sel_hi:[0,1]
	v_pk_mul_f32 v[6:7], v[30:31], v[6:7] op_sel_hi:[0,1]
	v_pk_mul_f32 v[8:9], v[30:31], v[8:9] op_sel_hi:[0,1]
	v_cmp_gt_u32_e32 vcc, s2, v10
	v_lshl_or_b32 v11, v10, 7, v1
	v_cvt_pk_f16_f32 v68, v2, v3
	v_cvt_pk_f16_f32 v69, v4, v5
	v_cvt_pk_f16_f32 v70, v6, v7
	v_cvt_pk_f16_f32 v71, v8, v9
	s_and_saveexec_b64 s[0:1], vcc
	global_store_dwordx4 v11, v[68:71], s[44:45]
	s_or_b64 exec, exec, s[0:1]
	v_cvt_f32_f16_e32 v2, v56
	v_cvt_f32_f16_sdwa v3, v56 dst_sel:DWORD dst_unused:UNUSED_PAD src0_sel:WORD_1
	v_cvt_f32_f16_e32 v4, v57
	v_cvt_f32_f16_sdwa v5, v57 dst_sel:DWORD dst_unused:UNUSED_PAD src0_sel:WORD_1
	v_cvt_f32_f16_e32 v6, v58
	v_cvt_f32_f16_sdwa v7, v58 dst_sel:DWORD dst_unused:UNUSED_PAD src0_sel:WORD_1
	v_cvt_f32_f16_e32 v8, v59
	v_cvt_f32_f16_sdwa v9, v59 dst_sel:DWORD dst_unused:UNUSED_PAD src0_sel:WORD_1
	v_add_u32_e32 v10, 0xc0, v24
	s_waitcnt lgkmcnt(0)
	v_pk_mul_f32 v[2:3], v[32:33], v[2:3] op_sel_hi:[0,1]
	v_pk_mul_f32 v[4:5], v[32:33], v[4:5] op_sel_hi:[0,1]
	v_pk_mul_f32 v[6:7], v[32:33], v[6:7] op_sel_hi:[0,1]
	v_pk_mul_f32 v[8:9], v[32:33], v[8:9] op_sel_hi:[0,1]
	v_cmp_gt_u32_e32 vcc, s2, v10
	v_lshl_or_b32 v11, v10, 7, v1
	v_cvt_pk_f16_f32 v56, v2, v3
	v_cvt_pk_f16_f32 v57, v4, v5
	v_cvt_pk_f16_f32 v58, v6, v7
	v_cvt_pk_f16_f32 v59, v8, v9
	s_and_saveexec_b64 s[0:1], vcc
	global_store_dwordx4 v11, v[56:59], s[44:45]
	s_or_b64 exec, exec, s[0:1]
	s_endpgm
	.section	.rodata,"a",@progbits
	.p2align	6, 0x0
